# P10: gate coefficient f16 pairs built with v_cvt_pk_f16_f32 from the f32 products (V-side step vector pre-scaled by 4096 once per token, exact) instead of fma_mixlo + and + lshl_or: 4 VALU fewer per 3
# speedup vs baseline: 1.0241x; 1.0002x over previous
; __device__ __forceinline__ void expert_tokens(const unsigned char* __restrict__ UV, const float* __restrict__ US, const float* __restrict__ VS, ...
;     ...
;         float sy = 0.f;
;         const float sumc = wave_sum(sumc_l) * (0.25f / 4096.f);
; #pragma unroll
;         for (int i = 0; i < 16; ++i) { acc[i] = acc[i] * 4096.f - 7.5f * sumc; sy += acc[i] * acc[i]; }
.LBB0_1013:
	v_add_f32_dpp v66, v252, v252 quad_perm:[1,0,3,2] row_mask:0xf bank_mask:0xf bound_ctrl:1
	s_ashr_i32 s21, s20, 31
	s_lshl_b64 s[4:5], s[20:21], 12
	v_add_f32_dpp v66, v66, v66 quad_perm:[2,3,0,1] row_mask:0xf bank_mask:0xf bound_ctrl:1
	v_lshl_add_u64 v[162:163], v[200:201], 0, s[4:5]
	s_waitcnt vmcnt(31)
	v_mov_b64_e32 v[190:191], v[80:81]
	v_add_f32_dpp v66, v66, v66 row_ror:4 row_mask:0xf bank_mask:0xf bound_ctrl:1
	s_waitcnt vmcnt(30)
	v_mov_b64_e32 v[186:187], v[76:77]
	s_waitcnt vmcnt(29)
	v_mov_b64_e32 v[182:183], v[88:89]
	v_add_f32_dpp v66, v66, v66 row_ror:8 row_mask:0xf bank_mask:0xf bound_ctrl:1
	v_mov_b32_e32 v67, v66
	s_nop 1
	v_permlane16_swap_b32_e32 v66, v67
	v_add_f32_e32 v66, v66, v67
	v_mov_b32_e32 v67, v66
	s_nop 1
	v_permlane32_swap_b32_e32 v66, v67
	v_add_f32_e32 v66, v66, v67
	v_mul_f32_e32 v66, 0x38800000, v66
	v_mul_f32_e32 v66, 0x40f00000, v66
	v_pk_add_f32 v[224:225], v[224:225], v[220:221] neg_lo:[0,1] neg_hi:[0,1]
	v_pk_add_f32 v[222:223], v[222:223], v[218:219] neg_lo:[0,1] neg_hi:[0,1]
	v_pk_add_f32 v[216:217], v[216:217], v[212:213] neg_lo:[0,1] neg_hi:[0,1]
	v_pk_add_f32 v[214:215], v[214:215], v[210:211] neg_lo:[0,1] neg_hi:[0,1]
	s_mov_b32 s62, 0x43800000
	v_pk_fma_f32 v[118:119], v[224:225], s[16:17], v[66:67] op_sel_hi:[1,0,0] neg_lo:[0,0,1] neg_hi:[0,0,1]
	v_pk_fma_f32 v[144:145], v[222:223], s[16:17], v[66:67] op_sel_hi:[1,0,0] neg_lo:[0,0,1] neg_hi:[0,0,1]
	v_pk_mul_f32 v[68:69], v[118:119], v[118:119]
	v_pk_mul_f32 v[70:71], v[144:145], v[144:145]
	v_add_f32_e32 v68, v68, v69
	v_pk_fma_f32 v[148:149], v[220:221], s[62:63], v[66:67] op_sel_hi:[1,0,0] neg_lo:[0,0,1] neg_hi:[0,0,1]
	v_add_f32_e32 v68, v70, v68
	v_pk_mul_f32 v[72:73], v[148:149], v[148:149]
	v_add_f32_e32 v68, v71, v68
	v_pk_fma_f32 v[150:151], v[218:219], s[62:63], v[66:67] op_sel_hi:[1,0,0] neg_lo:[0,0,1] neg_hi:[0,0,1]
	v_add_f32_e32 v68, v72, v68
	v_pk_mul_f32 v[114:115], v[150:151], v[150:151]
	v_add_f32_e32 v68, v73, v68
	v_pk_fma_f32 v[152:153], v[216:217], s[16:17], v[66:67] op_sel_hi:[1,0,0] neg_lo:[0,0,1] neg_hi:[0,0,1]
	v_add_f32_e32 v68, v114, v68
	v_pk_mul_f32 v[116:117], v[152:153], v[152:153]
	v_add_f32_e32 v68, v115, v68
	v_pk_fma_f32 v[154:155], v[214:215], s[16:17], v[66:67] op_sel_hi:[1,0,0] neg_lo:[0,0,1] neg_hi:[0,0,1]
	v_add_f32_e32 v68, v116, v68
	v_pk_mul_f32 v[146:147], v[154:155], v[154:155]
	v_add_f32_e32 v68, v117, v68
	v_pk_fma_f32 v[156:157], v[212:213], s[62:63], v[66:67] op_sel_hi:[1,0,0] neg_lo:[0,0,1] neg_hi:[0,0,1]
	v_add_f32_e32 v68, v146, v68
	v_pk_mul_f32 v[158:159], v[156:157], v[156:157]
	v_add_f32_e32 v68, v147, v68
	v_pk_fma_f32 v[160:161], v[210:211], s[62:63], v[66:67] op_sel_hi:[1,0,0] neg_lo:[0,0,1] neg_hi:[0,0,1]
	v_add_f32_e32 v68, v158, v68
	v_pk_mul_f32 v[66:67], v[160:161], v[160:161]
	v_add_f32_e32 v68, v159, v68
	v_add_f32_e32 v66, v66, v68
	v_add_f32_e32 v66, v67, v66
	ds_read_b128 v[114:117], v240 offset:8192
	ds_read2st64_b64 v[70:73], v239 offset0:34 offset1:35
	v_add_f32_dpp v66, v66, v66 quad_perm:[1,0,3,2] row_mask:0xf bank_mask:0xf bound_ctrl:1
	s_waitcnt vmcnt(28)
	v_mov_b64_e32 v[178:179], v[84:85]
	s_waitcnt vmcnt(27)
	v_mov_b64_e32 v[174:175], v[96:97]
	v_add_f32_dpp v66, v66, v66 quad_perm:[2,3,0,1] row_mask:0xf bank_mask:0xf bound_ctrl:1
	s_waitcnt vmcnt(26)
; #define LAS __attribute__((address_space(3)))
; __device__ __forceinline__ void expert_tokens(const unsigned char* __restrict__ UV, const float* __restrict__ US, const float* __restrict__ VS, ...
;     ...
;         const float ry = rsqrtf(wave_sum(sy) * (1.f / 1024.f) + EPS);
;         const float pscale = (t < 2048) ? 1.f + pd : 1.f;
; #pragma unroll
;         for (int j = 0; j < 4; ++j) { const f32x4 y = (f32x4){acc[4 * j], acc[4 * j + 1], acc[4 * j + 2], acc[4 * j + 3]};
;             float* op = out + (size_t)t * 1024 + 256 * j + 4 * lane;
;             const u32x2 xw = *(const LAS u32x2*)(xrow + 512 * j + 8 * lane);
;             { const f32x4 ov_ = pscale * (f32x4){__uint_as_float(xw.x << 16), __uint_as_float(xw.x & 0xffff0000u), __uint_as_float(xw.y << 16), __uint_as_float(xw.y & 0xffff0000u)} + pscale * *(const LAS f32x4*)(pvt + 2048 + 256 * j + 4 * lane) * (y * ry); __builtin_nontemporal_store(ov_, (f32x4*)op); } }
;         ci0 = ni0; ci1 = ni1; cg0 = ng0; cg1 = ng1; csu0 = nsu0; csu1 = nsu1; csv0 = nsv0; csv1 = nsv1;
	v_mov_b64_e32 v[170:171], v[92:93]
	v_mov_b64_e32 v[188:189], v[78:79]
	v_add_f32_dpp v66, v66, v66 row_ror:4 row_mask:0xf bank_mask:0xf bound_ctrl:1
	v_mov_b64_e32 v[184:185], v[74:75]
	v_mov_b64_e32 v[180:181], v[86:87]
	v_add_f32_dpp v66, v66, v66 row_ror:8 row_mask:0xf bank_mask:0xf bound_ctrl:1
	v_mov_b32_e32 v67, v66
	s_nop 1
	v_permlane16_swap_b32_e32 v66, v67
	v_add_f32_e32 v66, v66, v67
	v_mov_b32_e32 v67, v66
	s_nop 1
	v_permlane32_swap_b32_e32 v66, v67
	v_add_f32_e32 v66, v66, v67
	v_fmamk_f32 v66, v66, 0x3a800000, v226
	v_mul_f32_e32 v67, 0x4b800000, v66
	v_cmp_gt_f32_e32 vcc, s9, v66
	v_mov_b64_e32 v[176:177], v[82:83]
	v_mov_b64_e32 v[172:173], v[94:95]
	v_cndmask_b32_e32 v66, v66, v67, vcc
	v_rsq_f32_e32 v66, v66
	v_mov_b64_e32 v[168:169], v[90:91]
	s_mov_b64 s[92:93], s[86:87]
	s_mov_b64 s[86:87], s[88:89]
	s_mov_b64 s[88:89], s[92:93]
	v_mul_f32_e32 v67, 0x45800000, v66
	v_cndmask_b32_e32 v158, v66, v67, vcc
	ds_read2st64_b64 v[66:69], v239 offset0:32 offset1:33
	v_pk_mul_f32 v[166:167], v[144:145], v[158:159] op_sel_hi:[1,0]
	ds_read_b128 v[144:147], v240 offset:9216
	v_pk_mul_f32 v[118:119], v[118:119], v[158:159] op_sel_hi:[1,0]
	s_and_b64 vcc, exec, s[18:19]
	s_waitcnt lgkmcnt(1)
	v_lshlrev_b32_e32 v164, 16, v66
	v_and_b32_e32 v165, 0xffff0000, v66
	v_lshlrev_b32_e32 v66, 16, v67
	v_and_b32_e32 v67, 0xffff0000, v67
	v_pk_fma_f32 v[116:117], v[116:117], v[166:167], v[66:67]
	v_pk_fma_f32 v[114:115], v[114:115], v[118:119], v[164:165]
	global_store_dwordx4 v[162:163], v[114:117], off nt
	v_lshlrev_b32_e32 v66, 16, v68
	v_and_b32_e32 v67, 0xffff0000, v68
	v_lshlrev_b32_e32 v68, 16, v69
	v_and_b32_e32 v69, 0xffff0000, v69
	v_pk_mul_f32 v[114:115], v[148:149], v[158:159] op_sel_hi:[1,0]
	v_pk_mul_f32 v[116:117], v[150:151], v[158:159] op_sel_hi:[1,0]
	s_waitcnt lgkmcnt(0)
	v_pk_fma_f32 v[66:67], v[144:145], v[114:115], v[66:67]
	v_pk_fma_f32 v[68:69], v[146:147], v[116:117], v[68:69]
	global_store_dwordx4 v[162:163], v[66:69], off offset:1024 nt
	ds_read_b128 v[66:69], v240 offset:10240
	ds_read_b128 v[114:117], v240 offset:11264
	v_lshlrev_b32_e32 v118, 16, v70
	v_and_b32_e32 v119, 0xffff0000, v70
	v_lshlrev_b32_e32 v70, 16, v71
	v_and_b32_e32 v71, 0xffff0000, v71
	v_pk_mul_f32 v[144:145], v[152:153], v[158:159] op_sel_hi:[1,0]
	v_pk_mul_f32 v[146:147], v[154:155], v[158:159] op_sel_hi:[1,0]
	s_waitcnt lgkmcnt(1)
	v_pk_fma_f32 v[66:67], v[66:67], v[144:145], v[118:119]
	v_pk_fma_f32 v[68:69], v[68:69], v[146:147], v[70:71]
	global_store_dwordx4 v[162:163], v[66:69], off offset:2048 nt
	v_pk_mul_f32 v[70:71], v[156:157], v[158:159] op_sel_hi:[1,0]
	s_waitcnt vmcnt(28)
	v_mov_b64_e32 v[166:167], v[104:105]
	v_lshlrev_b32_e32 v66, 16, v72
	v_and_b32_e32 v67, 0xffff0000, v72
	v_lshlrev_b32_e32 v68, 16, v73
	v_and_b32_e32 v69, 0xffff0000, v73
	v_pk_mul_f32 v[72:73], v[160:161], v[158:159] op_sel_hi:[1,0]
	s_waitcnt lgkmcnt(0)
	v_pk_fma_f32 v[66:67], v[114:115], v[70:71], v[66:67]
	v_pk_fma_f32 v[68:69], v[116:117], v[72:73], v[68:69]
	s_waitcnt vmcnt(26)
	v_mov_b64_e32 v[158:159], v[112:113]
	global_store_dwordx4 v[162:163], v[66:69], off offset:3072 nt
	v_mov_b64_e32 v[162:163], v[100:101]
	v_mov_b64_e32 v[156:157], v[110:111]
	s_waitcnt vmcnt(26)
	v_mov_b64_e32 v[154:155], v[108:109]
	s_waitcnt vmcnt(25)
	v_mov_b64_e32 v[150:151], v[126:127]
	s_waitcnt vmcnt(24)
	v_mov_b64_e32 v[146:147], v[122:123]
	s_waitcnt vmcnt(23)
	v_mov_b64_e32 v[116:117], v[132:133]
	s_waitcnt vmcnt(22)
	v_mov_b64_e32 v[112:113], v[128:129]
	s_waitcnt vmcnt(21)
	v_mov_b64_e32 v[70:71], v[140:141]
	s_waitcnt vmcnt(20)
	v_mov_b64_e32 v[66:67], v[136:137]
	v_mov_b64_e32 v[164:165], v[102:103]
	v_mov_b64_e32 v[160:161], v[98:99]
	v_mov_b64_e32 v[152:153], v[106:107]
	v_mov_b64_e32 v[148:149], v[124:125]
	v_mov_b64_e32 v[144:145], v[120:121]
	v_mov_b64_e32 v[118:119], v[134:135]
	v_mov_b64_e32 v[114:115], v[130:131]
	v_mov_b64_e32 v[72:73], v[142:143]
	v_mov_b64_e32 v[68:69], v[138:139]
	v_mov_b32_e32 v229, v237
	v_mov_b32_e32 v230, v238
	v_mov_b32_e32 v233, v241
	v_mov_b32_e32 v234, v0
	v_mul_f32_e32 v235, s16, v245
	v_mul_f32_e32 v236, s16, v246
	s_mov_b32 s20, s34
	s_cbranch_vccnz .LBB0_1025

.Lp10_nobar_i:
	s_lshl_b32 s92, s21, 2
	s_cmp_lt_u32 s21, 0x80
	s_cselect_b32 s90, s86, s88
	s_cselect_b32 s91, s87, s89
	s_cselect_b32 s92, s92, 0
	s_add_u32 s90, s90, s92
	s_addc_u32 s91, s91, 0
	s_load_dwordx16 s[64:79], s[90:91], 0x0 glc
	v_dot8_i32_i4 v88, v248, v70, 0
	v_dot8_i32_i4 v88, v250, v71, v88
	s_nop 2
	v_lshlrev_b32_e32 v88, 4, v88
	v_dot8_i32_i4 v88, v247, v70, v88
	v_dot8_i32_i4 v74, v248, v188, 0
	v_dot8_i32_i4 v75, v248, v184, 0
	v_dot8_i32_i4 v76, v248, v180, 0
	v_dot8_i32_i4 v77, v248, v176, 0
	v_dot8_i32_i4 v78, v248, v172, 0
	v_dot8_i32_i4 v79, v248, v168, 0
	v_dot8_i32_i4 v80, v248, v164, 0
	v_dot8_i32_i4 v81, v248, v160, 0
	v_dot8_i32_i4 v82, v248, v156, 0
	v_dot8_i32_i4 v83, v248, v152, 0
	v_dot8_i32_i4 v84, v248, v148, 0
	v_dot8_i32_i4 v85, v248, v144, 0
	v_dot8_i32_i4 v86, v248, v116, 0
	v_dot8_i32_i4 v87, v248, v112, 0
	v_dot8_i32_i4 v70, v248, v66, 0
	v_dot8_i32_i4 v74, v250, v189, v74
	v_dot8_i32_i4 v75, v250, v185, v75
	v_dot8_i32_i4 v76, v250, v181, v76
	v_dot8_i32_i4 v77, v250, v177, v77
	v_dot8_i32_i4 v78, v250, v173, v78
	v_dot8_i32_i4 v79, v250, v169, v79
	v_dot8_i32_i4 v80, v250, v165, v80
	v_dot8_i32_i4 v81, v250, v161, v81
	v_dot8_i32_i4 v82, v250, v157, v82
	v_dot8_i32_i4 v83, v250, v153, v83
	v_dot8_i32_i4 v84, v250, v149, v84
	v_dot8_i32_i4 v85, v250, v145, v85
	v_dot8_i32_i4 v86, v250, v117, v86
	v_dot8_i32_i4 v87, v250, v113, v87
	v_dot8_i32_i4 v70, v250, v67, v70
	v_lshlrev_b32_e32 v74, 4, v74
	v_lshlrev_b32_e32 v75, 4, v75
	v_lshlrev_b32_e32 v76, 4, v76
	v_lshlrev_b32_e32 v77, 4, v77
	v_lshlrev_b32_e32 v78, 4, v78
	v_lshlrev_b32_e32 v79, 4, v79
	v_lshlrev_b32_e32 v80, 4, v80
	v_lshlrev_b32_e32 v81, 4, v81
	v_lshlrev_b32_e32 v82, 4, v82
	v_lshlrev_b32_e32 v83, 4, v83
	v_lshlrev_b32_e32 v84, 4, v84
	v_lshlrev_b32_e32 v85, 4, v85
	v_lshlrev_b32_e32 v86, 4, v86
	v_lshlrev_b32_e32 v87, 4, v87
	v_lshlrev_b32_e32 v70, 4, v70
	v_dot8_i32_i4 v74, v247, v188, v74
	v_dot8_i32_i4 v75, v247, v184, v75
	v_dot8_i32_i4 v76, v247, v180, v76
	v_dot8_i32_i4 v77, v247, v176, v77
	v_dot8_i32_i4 v78, v247, v172, v78
	v_dot8_i32_i4 v79, v247, v168, v79
	v_dot8_i32_i4 v80, v247, v164, v80
	v_dot8_i32_i4 v81, v247, v160, v81
	v_dot8_i32_i4 v82, v247, v156, v82
	v_dot8_i32_i4 v83, v247, v152, v83
	v_dot8_i32_i4 v84, v247, v148, v84
	v_dot8_i32_i4 v85, v247, v144, v85
	v_dot8_i32_i4 v86, v247, v116, v86
	v_dot8_i32_i4 v87, v247, v112, v87
	v_dot8_i32_i4 v70, v247, v66, v70
	v_dot8_i32_i4 v74, v249, v189, v74
	v_dot8_i32_i4 v75, v249, v185, v75
	v_dot8_i32_i4 v76, v249, v181, v76
	v_dot8_i32_i4 v77, v249, v177, v77
	v_dot8_i32_i4 v78, v249, v173, v78
	v_dot8_i32_i4 v79, v249, v169, v79
	v_dot8_i32_i4 v80, v249, v165, v80
	v_dot8_i32_i4 v81, v249, v161, v81
	v_dot8_i32_i4 v82, v249, v157, v82
	v_dot8_i32_i4 v83, v249, v153, v83
	v_dot8_i32_i4 v84, v249, v149, v84
	v_dot8_i32_i4 v85, v249, v145, v85
	v_dot8_i32_i4 v86, v249, v117, v86
	v_dot8_i32_i4 v87, v249, v113, v87
	v_dot8_i32_i4 v88, v249, v71, v88
	v_dot8_i32_i4 v70, v249, v67, v70
	v_permlane32_swap_b32_e32 v74, v82
	v_permlane32_swap_b32_e32 v75, v83
	v_permlane32_swap_b32_e32 v76, v84
	v_permlane32_swap_b32_e32 v77, v85
	v_permlane32_swap_b32_e32 v78, v86
	v_permlane32_swap_b32_e32 v79, v87
	v_permlane32_swap_b32_e32 v80, v88
	v_permlane32_swap_b32_e32 v81, v70
	v_add_u32_e32 v66, v74, v82
	v_add_u32_e32 v67, v75, v83
	v_add_u32_e32 v71, v76, v84
	v_add_u32_e32 v74, v77, v85
	v_add_u32_e32 v75, v78, v86
	v_add_u32_e32 v76, v79, v87
	v_add_u32_e32 v77, v80, v88
	v_add_u32_e32 v70, v81, v70
	v_permlane16_swap_b32_e32 v66, v75
	v_permlane16_swap_b32_e32 v67, v76
	v_permlane16_swap_b32_e32 v71, v77
	v_permlane16_swap_b32_e32 v74, v70
	v_add_u32_e32 v66, v66, v75
	v_add_u32_e32 v67, v67, v76
	v_add_u32_e32 v71, v71, v77
	v_add_u32_e32 v70, v74, v70
	v_cndmask_b32_e64 v74, v71, v66, s[0:1]
	v_cndmask_b32_e64 v66, v66, v71, s[0:1]
	v_cndmask_b32_e64 v71, v70, v67, s[0:1]
	v_cndmask_b32_e64 v67, v67, v70, s[0:1]
	v_add_u32_dpp v66, v66, v74 quad_perm:[2,3,0,1] row_mask:0xf bank_mask:0xf bound_ctrl:1
	s_sub_i32 s4, s21, 32
	v_add_u32_dpp v67, v67, v71 quad_perm:[2,3,0,1] row_mask:0xf bank_mask:0xf bound_ctrl:1
	v_cndmask_b32_e64 v70, v67, v66, s[2:3]
	v_cndmask_b32_e64 v66, v66, v67, s[2:3]
	s_cmp_lt_u32 s25, 4
	s_cselect_b64 vcc, -1, 0
	v_add_u32_dpp v66, v66, v70 quad_perm:[1,0,3,2] row_mask:0xf bank_mask:0xf bound_ctrl:1
	v_cndmask_b32_e32 v70, v234, v233, vcc
	v_cndmask_b32_e32 v71, v230, v229, vcc
	v_add_u32_dpp v66, v66, v66 row_ror:8 row_mask:0xf bank_mask:0xf bound_ctrl:1
	s_cmp_eq_u32 s21, 32
	s_nop 0
	v_add_u32_dpp v67, v66, v66 row_ror:4 row_mask:0xf bank_mask:0xf bound_ctrl:1
	v_and_or_b32 v66, s4, 32, v193
	v_lshlrev_b32_e32 v66, 2, v66
	v_cvt_f32_i32_e32 v74, v67
	s_waitcnt lgkmcnt(0)
	ds_bpermute_b32 v75, v66, v70
	v_and_b32_e32 v67, 0xffff0000, v71
	ds_bpermute_b32 v76, v66, v67
	v_add_f32_e32 v71, v251, v74
	v_mul_f32_e32 v71, v244, v71
	s_waitcnt lgkmcnt(1)
	v_mul_f32_e32 v74, v71, v75
	v_fma_f32 v71, |v74|, s28, 1.0
	v_rcp_f32_e32 v75, v71
	v_mul_f32_e32 v79, v74, v74
	v_mul_f32_e32 v79, 0xbf38aa3b, v79
	v_exp_f32_e32 v79, v79
	v_fmamk_f32 v78, v75, 0x3f07dc22, v227
	v_fmaak_f32 v78, v75, v78, 0x3f35f0e3
	v_fmaak_f32 v78, v75, v78, 0xbe11a98e
	v_cndmask_b32_e32 v71, v236, v235, vcc
	v_fmaak_f32 v78, v75, v78, 0x3e027906
	ds_bpermute_b32 v77, v66, v71
	v_mul_f32_e32 v75, v75, v78
	v_mul_f32_e32 v75, v79, v75
	v_mul_f32_e32 v78, v74, v75
	v_fma_f32 v75, -v74, v75, v74
	v_cmp_gt_f32_e32 vcc, 0, v74
	s_nop 1
	v_cndmask_b32_e32 v74, v75, v78, vcc
	s_waitcnt lgkmcnt(1)
	v_mul_f32_e32 v74, v74, v76
	s_cselect_b64 vcc, -1, 0
	s_cmp_gt_u32 s25, 5
	s_waitcnt lgkmcnt(0)
; __device__ __forceinline__ void expert_tokens(const unsigned char* __restrict__ UV, const float* __restrict__ US, const float* __restrict__ VS, ...
;     ...
;         const unsigned nw0 = (unsigned)IDX[(size_t)tn * 128 + lane], nw1 = (unsigned)IDX[(size_t)tn * 128 + 64 + lane];
;         const int ni0 = (int)nw0 & rmask, ni1 = (int)nw1 & rmask;
;         const float ng0 = __uint_as_float(nw0 & 0xFFFF0000u), ng1 = __uint_as_float(nw1 & 0xFFFF0000u);
	v_mul_f32_e32 v74, v74, v77
	s_cselect_b64 s[22:23], -1, 0
	s_cmp_lt_u32 s25, 6
	s_cselect_b64 s[4:5], -1, 0
	s_nop 1
	v_mov_b32_dpp v207, v74 quad_perm:[1,0,3,2] row_mask:0xf bank_mask:0xf
	s_cmp_lg_u32 s21, 32
	v_cvt_pk_f16_f32 v209, v74, v207
	v_cvt_f32_f16_e32 v116, v209
	s_nop 0
	v_readlane_b32 s47, v209, 0
	v_readlane_b32 s45, v209, 2
	v_readlane_b32 s43, v209, 16
	v_readlane_b32 s41, v209, 18
	v_readlane_b32 s39, v209, 32
	v_readlane_b32 s37, v209, 34
	v_readlane_b32 s35, v209, 48
	v_readlane_b32 s4, v209, 50
	buffer_load_dwordx4 v[78:81], v194, s[80:83], s64 offen
	buffer_load_dwordx4 v[74:77], v194, s[80:83], s65 offen
	buffer_load_dwordx4 v[86:89], v194, s[80:83], s66 offen
	buffer_load_dwordx4 v[82:85], v194, s[80:83], s67 offen
	buffer_load_dwordx4 v[94:97], v194, s[80:83], s68 offen
	buffer_load_dwordx4 v[90:93], v194, s[80:83], s69 offen
	buffer_load_dwordx4 v[102:105], v194, s[80:83], s70 offen
	buffer_load_dwordx4 v[98:101], v194, s[80:83], s71 offen
	buffer_load_dwordx4 v[110:113], v194, s[80:83], s72 offen
	buffer_load_dwordx4 v[106:109], v194, s[80:83], s73 offen
	buffer_load_dwordx4 v[124:127], v194, s[80:83], s74 offen
	buffer_load_dwordx4 v[120:123], v194, s[80:83], s75 offen
	buffer_load_dwordx4 v[132:135], v194, s[80:83], s76 offen
	buffer_load_dwordx4 v[128:131], v194, s[80:83], s77 offen
	buffer_load_dwordx4 v[140:143], v194, s[80:83], s78 offen
	buffer_load_dwordx4 v[136:139], v194, s[80:83], s79 offen
	s_cbranch_scc1 .LBB0_1021
	s_waitcnt vmcnt(16)
	s_bfe_i32 s60, s34, 0x10000
	v_alignbit_b32 v237, v237, v237, 16
	v_alignbit_b32 v238, v238, v238, 16
	v_xor_b32_e32 v237, s60, v237
	v_xor_b32_e32 v238, s60, v238
	s_nop 1
	s_mov_b32 s58, 0x99999999
	s_mov_b32 s59, 0x99999999
	v_min_u32_dpp v202, v237, v237 quad_perm:[1,0,3,2] row_mask:0xf bank_mask:0xf
	v_max_u32_dpp v203, v237, v237 quad_perm:[1,0,3,2] row_mask:0xf bank_mask:0xf
	v_min_u32_dpp v204, v238, v238 quad_perm:[1,0,3,2] row_mask:0xf bank_mask:0xf
	v_max_u32_dpp v205, v238, v238 quad_perm:[1,0,3,2] row_mask:0xf bank_mask:0xf
	v_cndmask_b32_e64 v237, v203, v202, s[58:59]
	v_cndmask_b32_e64 v238, v205, v204, s[58:59]
	s_mov_b32 s58, 0xcc33cc33
	s_mov_b32 s59, 0xcc33cc33
	v_min_u32_dpp v202, v237, v237 quad_perm:[2,3,0,1] row_mask:0xf bank_mask:0xf
	v_max_u32_dpp v203, v237, v237 quad_perm:[2,3,0,1] row_mask:0xf bank_mask:0xf
	v_min_u32_dpp v204, v238, v238 quad_perm:[2,3,0,1] row_mask:0xf bank_mask:0xf
	v_max_u32_dpp v205, v238, v238 quad_perm:[2,3,0,1] row_mask:0xf bank_mask:0xf
	v_cndmask_b32_e64 v237, v203, v202, s[58:59]
	v_cndmask_b32_e64 v238, v205, v204, s[58:59]
	s_mov_b32 s58, 0xaa55aa55
	s_mov_b32 s59, 0xaa55aa55
	v_min_u32_dpp v202, v237, v237 quad_perm:[1,0,3,2] row_mask:0xf bank_mask:0xf
	v_max_u32_dpp v203, v237, v237 quad_perm:[1,0,3,2] row_mask:0xf bank_mask:0xf
	v_min_u32_dpp v204, v238, v238 quad_perm:[1,0,3,2] row_mask:0xf bank_mask:0xf
	v_max_u32_dpp v205, v238, v238 quad_perm:[1,0,3,2] row_mask:0xf bank_mask:0xf
	v_cndmask_b32_e64 v237, v203, v202, s[58:59]
	v_cndmask_b32_e64 v238, v205, v204, s[58:59]
	s_mov_b32 s58, 0xf00ff00f
	s_mov_b32 s59, 0xf00ff00f
	v_min_u32_dpp v202, v237, v237 row_ror:8 row_mask:0xf bank_mask:0xf
	v_max_u32_dpp v203, v237, v237 row_ror:8 row_mask:0xf bank_mask:0xf
	v_min_u32_dpp v204, v238, v238 row_ror:8 row_mask:0xf bank_mask:0xf
	v_max_u32_dpp v205, v238, v238 row_ror:8 row_mask:0xf bank_mask:0xf
	v_cndmask_b32_e64 v237, v203, v202, s[58:59]
	v_cndmask_b32_e64 v238, v205, v204, s[58:59]
	s_mov_b32 s58, 0xc3c3c3c3
	s_mov_b32 s59, 0xc3c3c3c3
	v_min_u32_dpp v202, v237, v237 quad_perm:[2,3,0,1] row_mask:0xf bank_mask:0xf
	v_max_u32_dpp v203, v237, v237 quad_perm:[2,3,0,1] row_mask:0xf bank_mask:0xf
	v_min_u32_dpp v204, v238, v238 quad_perm:[2,3,0,1] row_mask:0xf bank_mask:0xf
	v_max_u32_dpp v205, v238, v238 quad_perm:[2,3,0,1] row_mask:0xf bank_mask:0xf
	v_cndmask_b32_e64 v237, v203, v202, s[58:59]
	v_cndmask_b32_e64 v238, v205, v204, s[58:59]
	s_mov_b32 s58, 0xa5a5a5a5
	s_mov_b32 s59, 0xa5a5a5a5
	v_min_u32_dpp v202, v237, v237 quad_perm:[1,0,3,2] row_mask:0xf bank_mask:0xf
	v_max_u32_dpp v203, v237, v237 quad_perm:[1,0,3,2] row_mask:0xf bank_mask:0xf
	v_min_u32_dpp v204, v238, v238 quad_perm:[1,0,3,2] row_mask:0xf bank_mask:0xf
	v_max_u32_dpp v205, v238, v238 quad_perm:[1,0,3,2] row_mask:0xf bank_mask:0xf
	v_cndmask_b32_e64 v237, v203, v202, s[58:59]
	v_cndmask_b32_e64 v238, v205, v204, s[58:59]
	s_mov_b32 s58, 0xf0f00f0f
	s_mov_b32 s59, 0xf0f00f0f
	v_mov_b32_dpp v202, v237 row_half_mirror row_mask:0xf bank_mask:0xf
	v_mov_b32_dpp v204, v238 row_half_mirror row_mask:0xf bank_mask:0xf
	s_nop 0
	v_max_u32_dpp v203, v202, v237 quad_perm:[3,2,1,0] row_mask:0xf bank_mask:0xf
	v_max_u32_dpp v205, v204, v238 quad_perm:[3,2,1,0] row_mask:0xf bank_mask:0xf
	v_min_u32_dpp v202, v202, v237 quad_perm:[3,2,1,0] row_mask:0xf bank_mask:0xf
	v_min_u32_dpp v204, v204, v238 quad_perm:[3,2,1,0] row_mask:0xf bank_mask:0xf
	v_cndmask_b32_e64 v237, v203, v202, s[58:59]
	v_cndmask_b32_e64 v238, v205, v204, s[58:59]
	s_mov_b32 s58, 0xff0000ff
	s_mov_b32 s59, 0xff0000ff
	v_min_u32_dpp v202, v237, v237 row_ror:8 row_mask:0xf bank_mask:0xf
	v_max_u32_dpp v203, v237, v237 row_ror:8 row_mask:0xf bank_mask:0xf
	v_min_u32_dpp v204, v238, v238 row_ror:8 row_mask:0xf bank_mask:0xf
	v_max_u32_dpp v205, v238, v238 row_ror:8 row_mask:0xf bank_mask:0xf
	v_cndmask_b32_e64 v237, v203, v202, s[58:59]
	v_cndmask_b32_e64 v238, v205, v204, s[58:59]
	s_mov_b32 s58, 0xcccc3333
	s_mov_b32 s59, 0xcccc3333
	v_min_u32_dpp v202, v237, v237 quad_perm:[2,3,0,1] row_mask:0xf bank_mask:0xf
	v_max_u32_dpp v203, v237, v237 quad_perm:[2,3,0,1] row_mask:0xf bank_mask:0xf
; __device__ __forceinline__ void expert_tokens(const unsigned char* __restrict__ UV, const float* __restrict__ US, const float* __restrict__ VS, ...
;     ...
;         const unsigned nw0 = (unsigned)IDX[(size_t)tn * 128 + lane], nw1 = (unsigned)IDX[(size_t)tn * 128 + 64 + lane];
;         const int ni0 = (int)nw0 & rmask, ni1 = (int)nw1 & rmask;
;         const float ng0 = __uint_as_float(nw0 & 0xFFFF0000u), ng1 = __uint_as_float(nw1 & 0xFFFF0000u);
;     ...
;             if (bi == 0) { nsu0 = US[ni0]; nsu1 = US[ni1]; nsv0 = VS[ni0]; nsv1 = VS[ni1]; }
	v_min_u32_dpp v204, v238, v238 quad_perm:[2,3,0,1] row_mask:0xf bank_mask:0xf
	v_max_u32_dpp v205, v238, v238 quad_perm:[2,3,0,1] row_mask:0xf bank_mask:0xf
	v_cndmask_b32_e64 v237, v203, v202, s[58:59]
	v_cndmask_b32_e64 v238, v205, v204, s[58:59]
	s_mov_b32 s58, 0xaaaa5555
	s_mov_b32 s59, 0xaaaa5555
	v_min_u32_dpp v202, v237, v237 quad_perm:[1,0,3,2] row_mask:0xf bank_mask:0xf
	v_max_u32_dpp v203, v237, v237 quad_perm:[1,0,3,2] row_mask:0xf bank_mask:0xf
	v_min_u32_dpp v204, v238, v238 quad_perm:[1,0,3,2] row_mask:0xf bank_mask:0xf
	v_max_u32_dpp v205, v238, v238 quad_perm:[1,0,3,2] row_mask:0xf bank_mask:0xf
	v_cndmask_b32_e64 v237, v203, v202, s[58:59]
	v_cndmask_b32_e64 v238, v205, v204, s[58:59]
	s_nop 1
	v_permlane16_swap_b32_e32 v237, v238
	s_mov_b32 s58, -1
	s_mov_b32 s59, 0
	v_min_u32_e32 v202, v237, v238
	v_max_u32_e32 v203, v237, v238
	v_cndmask_b32_e64 v237, v203, v202, s[58:59]
	v_cndmask_b32_e64 v238, v202, v203, s[58:59]
	s_mov_b32 s58, 0xf0f0f0f
	s_mov_b32 s59, 0xf0f0f0f0
	v_mov_b32_dpp v202, v237 row_half_mirror row_mask:0xf bank_mask:0xf
	v_mov_b32_dpp v204, v238 row_half_mirror row_mask:0xf bank_mask:0xf
	s_nop 0
	v_max_u32_dpp v203, v202, v237 quad_perm:[3,2,1,0] row_mask:0xf bank_mask:0xf
	v_max_u32_dpp v205, v204, v238 quad_perm:[3,2,1,0] row_mask:0xf bank_mask:0xf
	v_min_u32_dpp v202, v202, v237 quad_perm:[3,2,1,0] row_mask:0xf bank_mask:0xf
	v_min_u32_dpp v204, v204, v238 quad_perm:[3,2,1,0] row_mask:0xf bank_mask:0xf
	v_cndmask_b32_e64 v237, v203, v202, s[58:59]
	v_cndmask_b32_e64 v238, v205, v204, s[58:59]
	s_mov_b32 s58, 0xff00ff
	s_mov_b32 s59, 0xff00ff00
	v_min_u32_dpp v202, v237, v237 row_ror:8 row_mask:0xf bank_mask:0xf
	v_max_u32_dpp v203, v237, v237 row_ror:8 row_mask:0xf bank_mask:0xf
	v_min_u32_dpp v204, v238, v238 row_ror:8 row_mask:0xf bank_mask:0xf
	v_max_u32_dpp v205, v238, v238 row_ror:8 row_mask:0xf bank_mask:0xf
	v_cndmask_b32_e64 v237, v203, v202, s[58:59]
	v_cndmask_b32_e64 v238, v205, v204, s[58:59]
	s_mov_b32 s58, 0x33333333
	s_mov_b32 s59, 0xcccccccc
	v_min_u32_dpp v202, v237, v237 quad_perm:[2,3,0,1] row_mask:0xf bank_mask:0xf
	v_max_u32_dpp v203, v237, v237 quad_perm:[2,3,0,1] row_mask:0xf bank_mask:0xf
	v_min_u32_dpp v204, v238, v238 quad_perm:[2,3,0,1] row_mask:0xf bank_mask:0xf
	v_max_u32_dpp v205, v238, v238 quad_perm:[2,3,0,1] row_mask:0xf bank_mask:0xf
	v_cndmask_b32_e64 v237, v203, v202, s[58:59]
	v_cndmask_b32_e64 v238, v205, v204, s[58:59]
	s_mov_b32 s58, 0x55555555
	s_mov_b32 s59, 0xaaaaaaaa
	v_min_u32_dpp v202, v237, v237 quad_perm:[1,0,3,2] row_mask:0xf bank_mask:0xf
	v_max_u32_dpp v203, v237, v237 quad_perm:[1,0,3,2] row_mask:0xf bank_mask:0xf
	v_min_u32_dpp v204, v238, v238 quad_perm:[1,0,3,2] row_mask:0xf bank_mask:0xf
	v_max_u32_dpp v205, v238, v238 quad_perm:[1,0,3,2] row_mask:0xf bank_mask:0xf
	v_cndmask_b32_e64 v237, v203, v202, s[58:59]
	v_cndmask_b32_e64 v238, v205, v204, s[58:59]
	s_nop 1
	v_permlane32_swap_b32_e32 v237, v238
	s_mov_b32 s58, 0xffff
	s_mov_b32 s59, 0xffff
	v_min_u32_e32 v202, v237, v238
	v_max_u32_e32 v203, v237, v238
	v_cndmask_b32_e64 v237, v203, v202, s[58:59]
	v_cndmask_b32_e64 v238, v202, v203, s[58:59]
	s_nop 1
	v_permlane32_swap_b32_e32 v237, v238
	s_mov_b32 s58, 0xffff
	s_mov_b32 s59, 0xffff
	v_min_u32_e32 v202, v237, v238
	v_max_u32_e32 v203, v237, v238
	v_cndmask_b32_e64 v237, v203, v202, s[58:59]
	v_cndmask_b32_e64 v238, v202, v203, s[58:59]
	s_mov_b32 s58, 0xf0f00f0f
	s_mov_b32 s59, 0xf0f00f0f
	v_mov_b32_dpp v202, v237 row_half_mirror row_mask:0xf bank_mask:0xf
	v_mov_b32_dpp v204, v238 row_half_mirror row_mask:0xf bank_mask:0xf
	s_nop 0
	v_max_u32_dpp v203, v202, v237 quad_perm:[3,2,1,0] row_mask:0xf bank_mask:0xf
	v_max_u32_dpp v205, v204, v238 quad_perm:[3,2,1,0] row_mask:0xf bank_mask:0xf
	v_min_u32_dpp v202, v202, v237 quad_perm:[3,2,1,0] row_mask:0xf bank_mask:0xf
	v_min_u32_dpp v204, v204, v238 quad_perm:[3,2,1,0] row_mask:0xf bank_mask:0xf
	v_cndmask_b32_e64 v237, v203, v202, s[58:59]
	v_cndmask_b32_e64 v238, v205, v204, s[58:59]
	s_mov_b32 s58, 0xff0000ff
	s_mov_b32 s59, 0xff0000ff
	v_min_u32_dpp v202, v237, v237 row_ror:8 row_mask:0xf bank_mask:0xf
	v_max_u32_dpp v203, v237, v237 row_ror:8 row_mask:0xf bank_mask:0xf
	v_min_u32_dpp v204, v238, v238 row_ror:8 row_mask:0xf bank_mask:0xf
	v_max_u32_dpp v205, v238, v238 row_ror:8 row_mask:0xf bank_mask:0xf
	v_cndmask_b32_e64 v237, v203, v202, s[58:59]
	v_cndmask_b32_e64 v238, v205, v204, s[58:59]
	s_mov_b32 s58, 0xcccc3333
	s_mov_b32 s59, 0xcccc3333
	v_min_u32_dpp v202, v237, v237 quad_perm:[2,3,0,1] row_mask:0xf bank_mask:0xf
	v_max_u32_dpp v203, v237, v237 quad_perm:[2,3,0,1] row_mask:0xf bank_mask:0xf
	v_min_u32_dpp v204, v238, v238 quad_perm:[2,3,0,1] row_mask:0xf bank_mask:0xf
	v_max_u32_dpp v205, v238, v238 quad_perm:[2,3,0,1] row_mask:0xf bank_mask:0xf
	v_cndmask_b32_e64 v237, v203, v202, s[58:59]
	v_cndmask_b32_e64 v238, v205, v204, s[58:59]
	s_mov_b32 s58, 0xaaaa5555
	s_mov_b32 s59, 0xaaaa5555
	v_min_u32_dpp v202, v237, v237 quad_perm:[1,0,3,2] row_mask:0xf bank_mask:0xf
	v_max_u32_dpp v203, v237, v237 quad_perm:[1,0,3,2] row_mask:0xf bank_mask:0xf
	v_min_u32_dpp v204, v238, v238 quad_perm:[1,0,3,2] row_mask:0xf bank_mask:0xf
	v_max_u32_dpp v205, v238, v238 quad_perm:[1,0,3,2] row_mask:0xf bank_mask:0xf
	v_cndmask_b32_e64 v237, v203, v202, s[58:59]
	v_cndmask_b32_e64 v238, v205, v204, s[58:59]
	s_nop 1
	v_permlane16_swap_b32_e32 v237, v238
	v_min_u32_e32 v202, v237, v238
	v_max_u32_e32 v238, v237, v238
	v_mov_b32_e32 v237, v202
	s_nop 1
	v_permlane32_swap_b32_e32 v237, v238
	v_min_u32_e32 v202, v237, v238
	v_max_u32_e32 v238, v237, v238
	v_mov_b32_e32 v237, v202
	s_nop 1
	v_permlane16_swap_b32_e32 v237, v238
	v_min_u32_e32 v202, v237, v238
	v_max_u32_e32 v238, v237, v238
	v_mov_b32_e32 v237, v202
	s_nop 1
	v_permlane16_swap_b32_e32 v237, v238
	s_nop 1
	v_permlane32_swap_b32_e32 v237, v238
	v_xor_b32_e32 v237, s60, v237
	v_xor_b32_e32 v238, s60, v238
	v_alignbit_b32 v237, v237, v237, 16
	v_alignbit_b32 v238, v238, v238, 16
	v_and_b32_e32 v242, 0x3fff, v237
	v_and_b32_e32 v243, 0x3fff, v238
	v_lshlrev_b32_e32 v208, 2, v242
	v_lshlrev_b32_e32 v206, 2, v243
	v_lshlrev_b32_e32 v204, 10, v242
	v_lshlrev_b32_e32 v205, 10, v243
	global_store_dword v192, v204, s[88:89]
	global_store_dword v192, v205, s[88:89] offset:256
	global_load_dword v241, v208, s[12:13]
	global_load_dword v0, v206, s[12:13]
	global_load_dword v245, v208, s[14:15]
	global_load_dword v246, v206, s[14:15]
.LBB0_1021:
	s_lshl_b32 s92, s21, 2
	s_cmp_lt_u32 s21, 0x80
	s_cselect_b32 s90, s86, s88
	s_cselect_b32 s91, s87, s89
	s_cselect_b32 s92, s92, 0
	s_add_u32 s90, s90, s92
	s_addc_u32 s91, s91, 0
	s_load_dwordx16 s[64:79], s[90:91], 0x40 glc
	v_perm_b32 v149, v186, v190, s29
	v_dot2c_f32_f16_e32 v224, s47, v149
	v_and_b32_e32 v149, s32, v149
	v_dot2c_f32_f16_e32 v220, s47, v149
	v_perm_b32 v149, v186, v190, s30
	v_dot2c_f32_f16_e32 v225, s47, v149
	v_and_b32_e32 v149, s32, v149
	v_dot2c_f32_f16_e32 v221, s47, v149
	v_perm_b32 v149, v186, v190, s31
	v_perm_b32 v117, v186, v190, s33
	v_dot2c_f32_f16_e32 v223, s47, v117
	v_and_b32_e32 v117, s32, v117
	v_dot2c_f32_f16_e32 v222, s47, v149
	v_and_b32_e32 v149, s32, v149
	v_dot2c_f32_f16_e32 v219, s47, v117
	v_dot2c_f32_f16_e32 v218, s47, v149
	v_perm_b32 v149, v187, v191, s29
	v_dot2c_f32_f16_e32 v216, s47, v149
	v_and_b32_e32 v149, s32, v149
	v_dot2c_f32_f16_e32 v212, s47, v149
	v_perm_b32 v149, v187, v191, s30
	v_dot2c_f32_f16_e32 v217, s47, v149
	v_and_b32_e32 v149, s32, v149
	v_dot2c_f32_f16_e32 v213, s47, v149
	v_perm_b32 v149, v187, v191, s31
	v_perm_b32 v117, v187, v191, s33
	v_dot2c_f32_f16_e32 v215, s47, v117
	v_and_b32_e32 v117, s32, v117
	v_dot2c_f32_f16_e32 v214, s47, v149
	v_and_b32_e32 v149, s32, v149
	v_dot2c_f32_f16_e32 v211, s47, v117
	v_dot2c_f32_f16_e32 v210, s47, v149
	v_perm_b32 v149, v178, v182, s29
	v_dot2c_f32_f16_e32 v224, s45, v149
	v_and_b32_e32 v149, s32, v149
	v_dot2c_f32_f16_e32 v220, s45, v149
	v_perm_b32 v149, v178, v182, s30
	v_dot2c_f32_f16_e32 v225, s45, v149
	v_and_b32_e32 v149, s32, v149
	v_dot2c_f32_f16_e32 v221, s45, v149
	v_perm_b32 v149, v178, v182, s31
	v_perm_b32 v117, v178, v182, s33
	v_dot2c_f32_f16_e32 v223, s45, v117
	v_and_b32_e32 v117, s32, v117
	v_dot2c_f32_f16_e32 v222, s45, v149
	v_and_b32_e32 v149, s32, v149
	v_dot2c_f32_f16_e32 v219, s45, v117
	v_dot2c_f32_f16_e32 v218, s45, v149
	v_perm_b32 v149, v179, v183, s29
	v_dot2c_f32_f16_e32 v216, s45, v149
	v_and_b32_e32 v149, s32, v149
	v_dot2c_f32_f16_e32 v212, s45, v149
	v_perm_b32 v149, v179, v183, s30
	v_dot2c_f32_f16_e32 v217, s45, v149
	v_and_b32_e32 v149, s32, v149
	v_dot2c_f32_f16_e32 v213, s45, v149
	v_perm_b32 v149, v179, v183, s31
	v_perm_b32 v117, v179, v183, s33
	v_dot2c_f32_f16_e32 v215, s45, v117
	v_and_b32_e32 v117, s32, v117
	v_dot2c_f32_f16_e32 v214, s45, v149
	v_and_b32_e32 v149, s32, v149
	v_dot2c_f32_f16_e32 v211, s45, v117
	v_dot2c_f32_f16_e32 v210, s45, v149
	v_perm_b32 v149, v170, v174, s29
	v_dot2c_f32_f16_e32 v224, s43, v149
	v_and_b32_e32 v149, s32, v149
	v_dot2c_f32_f16_e32 v220, s43, v149
	v_perm_b32 v149, v170, v174, s30
	v_dot2c_f32_f16_e32 v225, s43, v149
	v_and_b32_e32 v149, s32, v149
	v_dot2c_f32_f16_e32 v221, s43, v149
	v_perm_b32 v149, v170, v174, s31
	v_perm_b32 v117, v170, v174, s33
	v_dot2c_f32_f16_e32 v223, s43, v117
	v_and_b32_e32 v117, s32, v117
	v_dot2c_f32_f16_e32 v222, s43, v149
	v_and_b32_e32 v149, s32, v149
	v_dot2c_f32_f16_e32 v219, s43, v117
	v_dot2c_f32_f16_e32 v218, s43, v149
	v_perm_b32 v149, v171, v175, s29
	v_dot2c_f32_f16_e32 v216, s43, v149
	v_and_b32_e32 v149, s32, v149
	v_dot2c_f32_f16_e32 v212, s43, v149
	v_perm_b32 v149, v171, v175, s30
	v_dot2c_f32_f16_e32 v217, s43, v149
	v_and_b32_e32 v149, s32, v149
	v_dot2c_f32_f16_e32 v213, s43, v149
	v_perm_b32 v149, v171, v175, s31
	v_perm_b32 v117, v171, v175, s33
	v_dot2c_f32_f16_e32 v215, s43, v117
	v_and_b32_e32 v117, s32, v117
	v_dot2c_f32_f16_e32 v214, s43, v149
	v_and_b32_e32 v149, s32, v149
	v_dot2c_f32_f16_e32 v211, s43, v117
	v_dot2c_f32_f16_e32 v210, s43, v149
	v_perm_b32 v149, v162, v166, s29
	v_dot2c_f32_f16_e32 v224, s41, v149
	v_and_b32_e32 v149, s32, v149
	v_dot2c_f32_f16_e32 v220, s41, v149
	v_perm_b32 v149, v162, v166, s30
	v_dot2c_f32_f16_e32 v225, s41, v149
	v_and_b32_e32 v149, s32, v149
	v_dot2c_f32_f16_e32 v221, s41, v149
	v_perm_b32 v149, v162, v166, s31
	v_perm_b32 v117, v162, v166, s33
	v_dot2c_f32_f16_e32 v223, s41, v117
	v_and_b32_e32 v117, s32, v117
	v_dot2c_f32_f16_e32 v222, s41, v149
	v_and_b32_e32 v149, s32, v149
	v_dot2c_f32_f16_e32 v219, s41, v117
	v_dot2c_f32_f16_e32 v218, s41, v149
	v_perm_b32 v149, v163, v167, s29
	v_dot2c_f32_f16_e32 v216, s41, v149
	v_and_b32_e32 v149, s32, v149
	v_dot2c_f32_f16_e32 v212, s41, v149
	v_perm_b32 v149, v163, v167, s30
	v_dot2c_f32_f16_e32 v217, s41, v149
	v_and_b32_e32 v149, s32, v149
	v_dot2c_f32_f16_e32 v213, s41, v149
	v_perm_b32 v149, v163, v167, s31
	v_perm_b32 v117, v163, v167, s33
	v_dot2c_f32_f16_e32 v215, s41, v117
	v_and_b32_e32 v117, s32, v117
	v_dot2c_f32_f16_e32 v214, s41, v149
	v_and_b32_e32 v149, s32, v149
	v_dot2c_f32_f16_e32 v211, s41, v117
	v_dot2c_f32_f16_e32 v210, s41, v149
	v_perm_b32 v149, v154, v158, s29
	v_dot2c_f32_f16_e32 v224, s39, v149
	v_and_b32_e32 v149, s32, v149
	v_dot2c_f32_f16_e32 v220, s39, v149
	v_perm_b32 v149, v154, v158, s30
	v_dot2c_f32_f16_e32 v225, s39, v149
	v_and_b32_e32 v149, s32, v149
	v_dot2c_f32_f16_e32 v221, s39, v149
	v_perm_b32 v149, v154, v158, s31
	v_perm_b32 v117, v154, v158, s33
	v_dot2c_f32_f16_e32 v223, s39, v117
	v_and_b32_e32 v117, s32, v117
	v_dot2c_f32_f16_e32 v222, s39, v149
	v_and_b32_e32 v149, s32, v149
	v_dot2c_f32_f16_e32 v219, s39, v117
	v_dot2c_f32_f16_e32 v218, s39, v149
	v_perm_b32 v149, v155, v159, s29
	v_dot2c_f32_f16_e32 v216, s39, v149
	v_and_b32_e32 v149, s32, v149
	v_dot2c_f32_f16_e32 v212, s39, v149
	v_perm_b32 v149, v155, v159, s30
	v_dot2c_f32_f16_e32 v217, s39, v149
	v_and_b32_e32 v149, s32, v149
	v_dot2c_f32_f16_e32 v213, s39, v149
	v_perm_b32 v149, v155, v159, s31
	v_perm_b32 v117, v155, v159, s33
	v_dot2c_f32_f16_e32 v215, s39, v117
	v_and_b32_e32 v117, s32, v117
	v_dot2c_f32_f16_e32 v214, s39, v149
	v_and_b32_e32 v149, s32, v149
	v_dot2c_f32_f16_e32 v211, s39, v117
	v_perm_b32 v148, v146, v150, s29
	v_dot2c_f32_f16_e32 v224, s37, v148
	v_and_b32_e32 v148, s32, v148
	v_dot2c_f32_f16_e32 v220, s37, v148
	v_perm_b32 v148, v146, v150, s30
	v_dot2c_f32_f16_e32 v225, s37, v148
	v_and_b32_e32 v148, s32, v148
	v_dot2c_f32_f16_e32 v221, s37, v148
	v_perm_b32 v148, v146, v150, s31
	v_perm_b32 v117, v146, v150, s33
	v_dot2c_f32_f16_e32 v223, s37, v117
	v_and_b32_e32 v117, s32, v117
	v_dot2c_f32_f16_e32 v222, s37, v148
	v_and_b32_e32 v148, s32, v148
	v_dot2c_f32_f16_e32 v219, s37, v117
	v_perm_b32 v207, v147, v151, s29
	v_dot2c_f32_f16_e32 v216, s37, v207
	v_and_b32_e32 v207, s32, v207
	v_dot2c_f32_f16_e32 v212, s37, v207
	v_perm_b32 v207, v147, v151, s30
	v_dot2c_f32_f16_e32 v217, s37, v207
	v_and_b32_e32 v207, s32, v207
	v_dot2c_f32_f16_e32 v213, s37, v207
	v_perm_b32 v207, v147, v151, s31
	v_perm_b32 v117, v147, v151, s33
	v_dot2c_f32_f16_e32 v215, s37, v117
	v_and_b32_e32 v117, s32, v117
	v_dot2c_f32_f16_e32 v214, s37, v207
	v_and_b32_e32 v207, s32, v207
	v_dot2c_f32_f16_e32 v211, s37, v117
	v_perm_b32 v145, v114, v118, s29
	v_dot2c_f32_f16_e32 v224, s35, v145
	v_and_b32_e32 v145, s32, v145
	v_dot2c_f32_f16_e32 v220, s35, v145
	v_perm_b32 v145, v114, v118, s30
	v_dot2c_f32_f16_e32 v225, s35, v145
	v_and_b32_e32 v145, s32, v145
	v_dot2c_f32_f16_e32 v221, s35, v145
	v_perm_b32 v145, v114, v118, s31
	v_dot2c_f32_f16_e32 v222, s35, v145
	v_and_b32_e32 v145, s32, v145
	v_perm_b32 v117, v114, v118, s33
	v_and_b32_e32 v209, s32, v117
	v_dot2c_f32_f16_e32 v223, s35, v117
	v_dot2c_f32_f16_e32 v219, s35, v209
	v_perm_b32 v253, v115, v119, s29
	v_dot2c_f32_f16_e32 v216, s35, v253
	v_and_b32_e32 v253, s32, v253
	v_dot2c_f32_f16_e32 v212, s35, v253
	v_perm_b32 v253, v115, v119, s30
	v_dot2c_f32_f16_e32 v217, s35, v253
	v_and_b32_e32 v253, s32, v253
	v_dot2c_f32_f16_e32 v213, s35, v253
	v_perm_b32 v253, v115, v119, s31
	v_perm_b32 v209, v115, v119, s33
	v_dot2c_f32_f16_e32 v215, s35, v209
	v_and_b32_e32 v209, s32, v209
	v_dot2c_f32_f16_e32 v214, s35, v253
	v_and_b32_e32 v253, s32, v253
	v_dot2c_f32_f16_e32 v211, s35, v209
	v_perm_b32 v117, v68, v72, s29
	v_dot2c_f32_f16_e32 v224, s4, v117
	v_and_b32_e32 v117, s32, v117
	v_dot2c_f32_f16_e32 v220, s4, v117
	v_perm_b32 v117, v68, v72, s30
	v_dot2c_f32_f16_e32 v225, s4, v117
	v_and_b32_e32 v117, s32, v117
	v_dot2c_f32_f16_e32 v221, s4, v117
	v_perm_b32 v117, v68, v72, s31
	v_dot2c_f32_f16_e32 v222, s4, v117
	v_and_b32_e32 v117, s32, v117
	v_perm_b32 v254, v68, v72, s33
	v_and_b32_e32 v254, s32, v254
	v_perm_b32 v209, v68, v72, s33
	v_dot2c_f32_f16_e32 v219, s4, v254
	v_dot2c_f32_f16_e32 v223, s4, v209
	v_perm_b32 v209, v69, v73, s29
	v_dot2c_f32_f16_e32 v216, s4, v209
	v_and_b32_e32 v209, s32, v209
	v_dot2c_f32_f16_e32 v212, s4, v209
	v_perm_b32 v209, v69, v73, s30
	v_dot2c_f32_f16_e32 v217, s4, v209
	v_and_b32_e32 v209, s32, v209
	v_dot2c_f32_f16_e32 v213, s4, v209
	v_perm_b32 v209, v69, v73, s31
	v_perm_b32 v254, v69, v73, s33
	v_dot2c_f32_f16_e32 v215, s4, v254
	s_waitcnt vmcnt(31)
	v_dot8_i32_i4 v68, v248, v62, 0
	v_dot8_i32_i4 v68, v250, v63, v68
	v_dot2c_f32_f16_e32 v210, s39, v149
	v_dot2c_f32_f16_e32 v218, s37, v148
	v_dot2c_f32_f16_e32 v210, s37, v207
	v_lshlrev_b32_e32 v68, 4, v68
	v_dot8_i32_i4 v68, v247, v62, v68
	s_waitcnt vmcnt(30)
	v_dot8_i32_i4 v62, v248, v58, 0
	v_dot8_i32_i4 v62, v250, v59, v62
	v_dot8_i32_i4 v68, v249, v63, v68
	v_dot2c_f32_f16_e32 v218, s35, v145
	v_dot2c_f32_f16_e32 v210, s35, v253
	v_lshlrev_b32_e32 v62, 4, v62
	v_dot8_i32_i4 v62, v247, v58, v62
	s_waitcnt vmcnt(29)
	v_dot8_i32_i4 v58, v248, v54, 0
	v_dot8_i32_i4 v58, v250, v55, v58
	v_dot8_i32_i4 v62, v249, v59, v62
	v_dot2c_f32_f16_e32 v214, s4, v209
	v_and_b32_e32 v209, s32, v209
	v_lshlrev_b32_e32 v58, 4, v58
	v_dot8_i32_i4 v58, v247, v54, v58
	s_waitcnt vmcnt(28)
	v_dot8_i32_i4 v54, v248, v50, 0
	v_dot8_i32_i4 v54, v250, v51, v54
	v_dot8_i32_i4 v58, v249, v55, v58
	v_dot2c_f32_f16_e32 v218, s4, v117
	v_dot2c_f32_f16_e32 v210, s4, v209
	v_lshlrev_b32_e32 v54, 4, v54
	v_dot8_i32_i4 v54, v247, v50, v54
	s_waitcnt vmcnt(27)
	v_dot8_i32_i4 v50, v248, v46, 0
	v_dot8_i32_i4 v50, v250, v47, v50
	v_dot8_i32_i4 v54, v249, v51, v54
	s_add_i32 s24, s25, 2
	s_cmp_lt_u32 s25, 5
	v_lshlrev_b32_e32 v50, 4, v50
	v_dot8_i32_i4 v50, v247, v46, v50
	s_waitcnt vmcnt(26)
	v_dot8_i32_i4 v46, v248, v42, 0
	v_dot8_i32_i4 v46, v250, v43, v46
	v_dot8_i32_i4 v50, v249, v47, v50
	s_nop 0
	s_nop 0
	v_lshlrev_b32_e32 v46, 4, v46
	v_dot8_i32_i4 v46, v247, v42, v46
	s_waitcnt vmcnt(25)
	v_dot8_i32_i4 v42, v248, v38, 0
	v_dot8_i32_i4 v42, v250, v39, v42
	v_dot8_i32_i4 v46, v249, v43, v46
	s_nop 1
	v_lshlrev_b32_e32 v42, 4, v42
	v_dot8_i32_i4 v42, v247, v38, v42
	s_waitcnt vmcnt(24)
	v_dot8_i32_i4 v38, v248, v30, 0
	v_dot8_i32_i4 v38, v250, v31, v38
	v_dot8_i32_i4 v42, v249, v39, v42
	s_nop 1
	v_lshlrev_b32_e32 v38, 4, v38
	v_dot8_i32_i4 v38, v247, v30, v38
	v_dot8_i32_i4 v38, v249, v31, v38
	s_waitcnt vmcnt(22)
	v_dot8_i32_i4 v31, v248, v22, 0
	v_dot8_i32_i4 v31, v250, v23, v31
	v_dot8_i32_i4 v30, v248, v34, 0
	v_dot8_i32_i4 v30, v250, v35, v30
	s_nop 0
	v_lshlrev_b32_e32 v31, 4, v31
	v_dot8_i32_i4 v31, v247, v22, v31
	v_dot8_i32_i4 v31, v249, v23, v31
	s_waitcnt vmcnt(20)
	v_dot8_i32_i4 v23, v248, v14, 0
	v_dot8_i32_i4 v23, v250, v15, v23
	v_dot8_i32_i4 v22, v248, v26, 0
	v_dot8_i32_i4 v22, v250, v27, v22
	s_nop 0
	v_lshlrev_b32_e32 v23, 4, v23
	v_dot8_i32_i4 v23, v247, v14, v23
	v_dot8_i32_i4 v23, v249, v15, v23
	s_waitcnt vmcnt(18)
	v_dot8_i32_i4 v15, v248, v6, 0
	v_dot8_i32_i4 v15, v250, v7, v15
	v_dot8_i32_i4 v14, v248, v18, 0
	v_dot8_i32_i4 v14, v250, v19, v14
	s_nop 0
	v_lshlrev_b32_e32 v15, 4, v15
	v_dot8_i32_i4 v15, v247, v6, v15
	v_dot8_i32_i4 v15, v249, v7, v15
	s_waitcnt vmcnt(17)
	v_dot8_i32_i4 v6, v248, v10, 0
	s_waitcnt vmcnt(16)
	v_dot8_i32_i4 v7, v248, v2, 0
	v_dot8_i32_i4 v6, v250, v11, v6
	v_dot8_i32_i4 v7, v250, v3, v7
	v_lshlrev_b32_e32 v30, 4, v30
	v_lshlrev_b32_e32 v22, 4, v22
	v_lshlrev_b32_e32 v14, 4, v14
	v_lshlrev_b32_e32 v6, 4, v6
	v_lshlrev_b32_e32 v7, 4, v7
	v_dot8_i32_i4 v30, v247, v34, v30
	v_dot8_i32_i4 v22, v247, v26, v22
	v_dot8_i32_i4 v14, v247, v18, v14
	v_dot8_i32_i4 v6, v247, v10, v6
	v_dot8_i32_i4 v7, v247, v2, v7
	v_dot8_i32_i4 v30, v249, v35, v30
	v_dot8_i32_i4 v22, v249, v27, v22
	v_dot8_i32_i4 v14, v249, v19, v14
	v_dot8_i32_i4 v6, v249, v11, v6
	v_dot8_i32_i4 v7, v249, v3, v7
	v_permlane32_swap_b32_e32 v68, v30
	v_permlane32_swap_b32_e32 v62, v31
	v_permlane32_swap_b32_e32 v58, v22
	v_permlane32_swap_b32_e32 v54, v23
	v_permlane32_swap_b32_e32 v50, v14
	v_permlane32_swap_b32_e32 v46, v15
	v_permlane32_swap_b32_e32 v42, v6
	v_permlane32_swap_b32_e32 v38, v7
	v_add_u32_e32 v2, v68, v30
	v_add_u32_e32 v3, v62, v31
	v_add_u32_e32 v10, v58, v22
	v_add_u32_e32 v11, v54, v23
	v_add_u32_e32 v14, v50, v14
	v_add_u32_e32 v15, v46, v15
	v_add_u32_e32 v6, v42, v6
	v_add_u32_e32 v7, v38, v7
	v_permlane16_swap_b32_e32 v2, v14
	v_permlane16_swap_b32_e32 v3, v15
	v_permlane16_swap_b32_e32 v10, v6
	v_permlane16_swap_b32_e32 v11, v7
	v_add_u32_e32 v2, v2, v14
	v_add_u32_e32 v3, v3, v15
	v_add_u32_e32 v6, v10, v6
	v_add_u32_e32 v7, v11, v7
	v_cndmask_b32_e64 v10, v6, v2, s[0:1]
	v_cndmask_b32_e64 v2, v2, v6, s[0:1]
	v_cndmask_b32_e64 v6, v7, v3, s[0:1]
	v_cndmask_b32_e64 v3, v3, v7, s[0:1]
	v_add_u32_dpp v2, v2, v10 quad_perm:[2,3,0,1] row_mask:0xf bank_mask:0xf bound_ctrl:1
	s_waitcnt lgkmcnt(0)
	ds_bpermute_b32 v7, v66, v71 offset:64
	v_add_u32_dpp v3, v3, v6 quad_perm:[2,3,0,1] row_mask:0xf bank_mask:0xf bound_ctrl:1
	v_cndmask_b32_e64 v6, v3, v2, s[2:3]
	v_cndmask_b32_e64 v2, v2, v3, s[2:3]
	ds_bpermute_b32 v3, v66, v70 offset:64
	v_add_f32_e32 v68, v252, v116
	v_add_u32_dpp v2, v2, v6 quad_perm:[1,0,3,2] row_mask:0xf bank_mask:0xf bound_ctrl:1
	v_and_b32_e32 v6, s32, v254
	v_dot2c_f32_f16_e32 v211, s4, v6
	v_add_u32_dpp v2, v2, v2 row_ror:8 row_mask:0xf bank_mask:0xf bound_ctrl:1
	ds_bpermute_b32 v6, v66, v67 offset:64
	s_nop 0
	v_add_u32_dpp v2, v2, v2 row_ror:4 row_mask:0xf bank_mask:0xf bound_ctrl:1
	v_cvt_f32_i32_e32 v2, v2
	v_add_f32_e32 v2, v251, v2
	v_mul_f32_e32 v2, v244, v2
	s_waitcnt lgkmcnt(1)
	v_mul_f32_e32 v2, v2, v3
	v_fma_f32 v3, |v2|, s28, 1.0
	v_rcp_f32_e32 v3, v3
	v_mul_f32_e32 v11, v2, v2
	v_mul_f32_e32 v11, 0xbf38aa3b, v11
	v_exp_f32_e32 v11, v11
	v_fmamk_f32 v10, v3, 0x3f07dc22, v227
	v_fmaak_f32 v10, v3, v10, 0x3f35f0e3
	v_fmaak_f32 v10, v3, v10, 0xbe11a98e
	v_fmaak_f32 v10, v3, v10, 0x3e027906
	v_mul_f32_e32 v3, v3, v10
	v_mul_f32_e32 v3, v11, v3
	v_mul_f32_e32 v10, v2, v3
	v_fma_f32 v3, -v2, v3, v2
	v_cmp_gt_f32_e64 s[4:5], 0, v2
	s_nop 1
	v_cndmask_b32_e64 v2, v3, v10, s[4:5]
	s_waitcnt lgkmcnt(0)
	v_mul_f32_e32 v2, v2, v6
	v_mul_f32_e32 v2, v2, v7
	s_cselect_b64 s[4:5], -1, 0
	s_nop 0
	v_mov_b32_dpp v253, v2 quad_perm:[1,0,3,2] row_mask:0xf bank_mask:0xf
	v_cvt_pk_f16_f32 v254, v2, v253
	v_cvt_f32_f16_e32 v66, v254
	v_readlane_b32 s5, v254, 0
	v_perm_b32 v14, v60, v64, s29
	s_nop 0
	v_dot2c_f32_f16_e32 v224, s5, v14
	v_and_b32_e32 v14, s32, v14
	v_dot2c_f32_f16_e32 v220, s5, v14
	v_perm_b32 v14, v60, v64, s30
	v_dot2c_f32_f16_e32 v225, s5, v14
	v_and_b32_e32 v14, s32, v14
	v_dot2c_f32_f16_e32 v221, s5, v14
	v_perm_b32 v14, v60, v64, s31
	v_perm_b32 v6, v60, v64, s33
	v_dot2c_f32_f16_e32 v223, s5, v6
	v_and_b32_e32 v6, s32, v6
	v_dot2c_f32_f16_e32 v222, s5, v14
	v_and_b32_e32 v14, s32, v14
	v_dot2c_f32_f16_e32 v219, s5, v6
	v_dot2c_f32_f16_e32 v218, s5, v14
	v_perm_b32 v14, v61, v65, s29
	v_dot2c_f32_f16_e32 v216, s5, v14
	v_and_b32_e32 v14, s32, v14
	v_dot2c_f32_f16_e32 v212, s5, v14
	v_perm_b32 v14, v61, v65, s30
	v_dot2c_f32_f16_e32 v217, s5, v14
	v_and_b32_e32 v14, s32, v14
	v_dot2c_f32_f16_e32 v213, s5, v14
	v_perm_b32 v14, v61, v65, s31
	v_perm_b32 v6, v61, v65, s33
	v_dot2c_f32_f16_e32 v214, s5, v14
	v_and_b32_e32 v14, s32, v14
	v_dot2c_f32_f16_e32 v215, s5, v6
	v_and_b32_e32 v6, s32, v6
	v_dot2c_f32_f16_e32 v210, s5, v14
	v_dot2c_f32_f16_e32 v211, s5, v6
	v_readlane_b32 s4, v254, 2
	buffer_load_dwordx4 v[62:65], v194, s[80:83], s64 offen
	buffer_load_dwordx4 v[58:61], v194, s[80:83], s65 offen
	v_perm_b32 v14, v52, v56, s29
	v_dot2c_f32_f16_e32 v224, s4, v14
	v_and_b32_e32 v14, s32, v14
	v_dot2c_f32_f16_e32 v220, s4, v14
	v_perm_b32 v14, v52, v56, s30
	v_dot2c_f32_f16_e32 v225, s4, v14
	v_and_b32_e32 v14, s32, v14
	v_dot2c_f32_f16_e32 v221, s4, v14
	v_perm_b32 v14, v52, v56, s31
	v_perm_b32 v6, v52, v56, s33
	v_dot2c_f32_f16_e32 v223, s4, v6
	v_and_b32_e32 v6, s32, v6
	v_dot2c_f32_f16_e32 v222, s4, v14
	v_and_b32_e32 v14, s32, v14
	v_dot2c_f32_f16_e32 v219, s4, v6
	v_dot2c_f32_f16_e32 v218, s4, v14
	v_perm_b32 v14, v53, v57, s29
	v_dot2c_f32_f16_e32 v216, s4, v14
	v_and_b32_e32 v14, s32, v14
	v_dot2c_f32_f16_e32 v212, s4, v14
	v_perm_b32 v14, v53, v57, s30
	v_dot2c_f32_f16_e32 v217, s4, v14
	v_and_b32_e32 v14, s32, v14
	v_dot2c_f32_f16_e32 v213, s4, v14
	v_perm_b32 v14, v53, v57, s31
	v_perm_b32 v6, v53, v57, s33
	v_dot2c_f32_f16_e32 v214, s4, v14
	v_and_b32_e32 v14, s32, v14
	v_dot2c_f32_f16_e32 v215, s4, v6
	v_and_b32_e32 v6, s32, v6
	v_dot2c_f32_f16_e32 v210, s4, v14
	v_dot2c_f32_f16_e32 v211, s4, v6
	v_readlane_b32 s4, v254, 16
	buffer_load_dwordx4 v[54:57], v194, s[80:83], s66 offen
	buffer_load_dwordx4 v[50:53], v194, s[80:83], s67 offen
	v_perm_b32 v14, v44, v48, s29
	v_dot2c_f32_f16_e32 v224, s4, v14
	v_and_b32_e32 v14, s32, v14
	v_dot2c_f32_f16_e32 v220, s4, v14
	v_perm_b32 v14, v44, v48, s30
	v_dot2c_f32_f16_e32 v225, s4, v14
	v_and_b32_e32 v14, s32, v14
	v_dot2c_f32_f16_e32 v221, s4, v14
	v_perm_b32 v14, v44, v48, s31
	v_perm_b32 v6, v44, v48, s33
	v_dot2c_f32_f16_e32 v223, s4, v6
	v_and_b32_e32 v6, s32, v6
	v_dot2c_f32_f16_e32 v222, s4, v14
	v_and_b32_e32 v14, s32, v14
	v_dot2c_f32_f16_e32 v219, s4, v6
	v_dot2c_f32_f16_e32 v218, s4, v14
	v_perm_b32 v14, v45, v49, s29
	v_dot2c_f32_f16_e32 v216, s4, v14
	v_and_b32_e32 v14, s32, v14
	v_dot2c_f32_f16_e32 v212, s4, v14
	v_perm_b32 v14, v45, v49, s30
	v_dot2c_f32_f16_e32 v217, s4, v14
	v_and_b32_e32 v14, s32, v14
	v_dot2c_f32_f16_e32 v213, s4, v14
	v_perm_b32 v14, v45, v49, s31
	v_perm_b32 v6, v45, v49, s33
	v_dot2c_f32_f16_e32 v214, s4, v14
	v_and_b32_e32 v14, s32, v14
	v_dot2c_f32_f16_e32 v215, s4, v6
	v_and_b32_e32 v6, s32, v6
	v_dot2c_f32_f16_e32 v210, s4, v14
	v_dot2c_f32_f16_e32 v211, s4, v6
	v_readlane_b32 s4, v254, 18
	buffer_load_dwordx4 v[46:49], v194, s[80:83], s68 offen
	buffer_load_dwordx4 v[42:45], v194, s[80:83], s69 offen
	v_perm_b32 v14, v32, v40, s29
	v_dot2c_f32_f16_e32 v224, s4, v14
	v_and_b32_e32 v14, s32, v14
	v_dot2c_f32_f16_e32 v220, s4, v14
	v_perm_b32 v14, v32, v40, s30
	v_dot2c_f32_f16_e32 v225, s4, v14
	v_and_b32_e32 v14, s32, v14
	v_dot2c_f32_f16_e32 v221, s4, v14
	v_perm_b32 v14, v32, v40, s31
	v_perm_b32 v6, v32, v40, s33
	v_dot2c_f32_f16_e32 v223, s4, v6
	v_and_b32_e32 v6, s32, v6
	v_dot2c_f32_f16_e32 v222, s4, v14
	v_and_b32_e32 v14, s32, v14
	v_dot2c_f32_f16_e32 v219, s4, v6
	v_dot2c_f32_f16_e32 v218, s4, v14
	v_perm_b32 v14, v33, v41, s29
	v_dot2c_f32_f16_e32 v216, s4, v14
	v_and_b32_e32 v14, s32, v14
	v_dot2c_f32_f16_e32 v212, s4, v14
	v_perm_b32 v14, v33, v41, s30
	v_dot2c_f32_f16_e32 v217, s4, v14
	v_and_b32_e32 v14, s32, v14
	v_dot2c_f32_f16_e32 v213, s4, v14
	v_perm_b32 v14, v33, v41, s31
	v_perm_b32 v6, v33, v41, s33
	v_dot2c_f32_f16_e32 v214, s4, v14
	v_and_b32_e32 v14, s32, v14
	v_dot2c_f32_f16_e32 v215, s4, v6
	v_and_b32_e32 v6, s32, v6
	v_dot2c_f32_f16_e32 v210, s4, v14
	v_dot2c_f32_f16_e32 v211, s4, v6
	v_readlane_b32 s4, v254, 32
	buffer_load_dwordx4 v[38:41], v194, s[80:83], s70 offen
	buffer_load_dwordx4 v[30:33], v194, s[80:83], s71 offen
	v_perm_b32 v14, v24, v36, s29
	v_dot2c_f32_f16_e32 v224, s4, v14
	v_and_b32_e32 v14, s32, v14
	v_dot2c_f32_f16_e32 v220, s4, v14
	v_perm_b32 v14, v24, v36, s30
	v_dot2c_f32_f16_e32 v225, s4, v14
	v_and_b32_e32 v14, s32, v14
	v_dot2c_f32_f16_e32 v221, s4, v14
	v_perm_b32 v14, v24, v36, s31
	v_perm_b32 v6, v24, v36, s33
	v_dot2c_f32_f16_e32 v223, s4, v6
	v_and_b32_e32 v6, s32, v6
	v_dot2c_f32_f16_e32 v222, s4, v14
	v_and_b32_e32 v14, s32, v14
	v_dot2c_f32_f16_e32 v219, s4, v6
	v_dot2c_f32_f16_e32 v218, s4, v14
	v_perm_b32 v14, v25, v37, s29
	v_dot2c_f32_f16_e32 v216, s4, v14
	v_and_b32_e32 v14, s32, v14
	v_dot2c_f32_f16_e32 v212, s4, v14
	v_perm_b32 v14, v25, v37, s30
	v_dot2c_f32_f16_e32 v217, s4, v14
	v_and_b32_e32 v14, s32, v14
	v_dot2c_f32_f16_e32 v213, s4, v14
	v_perm_b32 v14, v25, v37, s31
	v_perm_b32 v6, v25, v37, s33
	v_dot2c_f32_f16_e32 v214, s4, v14
	v_and_b32_e32 v14, s32, v14
	v_dot2c_f32_f16_e32 v215, s4, v6
	v_and_b32_e32 v6, s32, v6
	v_dot2c_f32_f16_e32 v210, s4, v14
	v_dot2c_f32_f16_e32 v211, s4, v6
	v_readlane_b32 s4, v254, 34
	buffer_load_dwordx4 v[34:37], v194, s[80:83], s72 offen
	buffer_load_dwordx4 v[22:25], v194, s[80:83], s73 offen
	v_perm_b32 v14, v16, v28, s29
	v_dot2c_f32_f16_e32 v224, s4, v14
	v_and_b32_e32 v14, s32, v14
	v_dot2c_f32_f16_e32 v220, s4, v14
	v_perm_b32 v14, v16, v28, s30
	v_dot2c_f32_f16_e32 v225, s4, v14
	v_and_b32_e32 v14, s32, v14
	v_dot2c_f32_f16_e32 v221, s4, v14
	v_perm_b32 v14, v16, v28, s31
	v_perm_b32 v6, v16, v28, s33
	v_dot2c_f32_f16_e32 v223, s4, v6
	v_and_b32_e32 v6, s32, v6
	v_dot2c_f32_f16_e32 v222, s4, v14
	v_and_b32_e32 v14, s32, v14
	v_dot2c_f32_f16_e32 v219, s4, v6
	v_dot2c_f32_f16_e32 v218, s4, v14
	v_perm_b32 v14, v17, v29, s29
	v_dot2c_f32_f16_e32 v216, s4, v14
; __device__ __forceinline__ void expert_tokens(const unsigned char* __restrict__ UV, const float* __restrict__ US, const float* __restrict__ VS, ...
;     ...
;         for (int bi = 0; bi < 128 / EB; bi += 2) {
;             EXP_STEP(A, bi);
;             if (bi == 0) { nsu0 = US[ni0]; nsu1 = US[ni1]; nsv0 = VS[ni0]; nsv1 = VS[ni1]; }
;             EXP_STEP(B, bi + 1);
;         }
	v_and_b32_e32 v14, s32, v14
	v_dot2c_f32_f16_e32 v212, s4, v14
	v_perm_b32 v14, v17, v29, s30
	v_dot2c_f32_f16_e32 v217, s4, v14
	v_and_b32_e32 v14, s32, v14
	v_dot2c_f32_f16_e32 v213, s4, v14
	v_perm_b32 v14, v17, v29, s31
	v_perm_b32 v6, v17, v29, s33
	v_dot2c_f32_f16_e32 v214, s4, v14
	v_and_b32_e32 v14, s32, v14
	v_dot2c_f32_f16_e32 v215, s4, v6
	v_and_b32_e32 v6, s32, v6
	v_dot2c_f32_f16_e32 v210, s4, v14
	v_dot2c_f32_f16_e32 v211, s4, v6
	v_readlane_b32 s4, v254, 48
	buffer_load_dwordx4 v[26:29], v194, s[80:83], s74 offen
	buffer_load_dwordx4 v[14:17], v194, s[80:83], s75 offen
	v_perm_b32 v11, v8, v20, s29
	v_dot2c_f32_f16_e32 v224, s4, v11
	v_and_b32_e32 v11, s32, v11
	v_dot2c_f32_f16_e32 v220, s4, v11
	v_perm_b32 v11, v8, v20, s30
	v_dot2c_f32_f16_e32 v225, s4, v11
	v_and_b32_e32 v11, s32, v11
	v_dot2c_f32_f16_e32 v221, s4, v11
	v_perm_b32 v11, v8, v20, s31
	v_perm_b32 v6, v8, v20, s33
	v_dot2c_f32_f16_e32 v223, s4, v6
	v_and_b32_e32 v6, s32, v6
	v_dot2c_f32_f16_e32 v222, s4, v11
	v_and_b32_e32 v11, s32, v11
	v_dot2c_f32_f16_e32 v219, s4, v6
	v_perm_b32 v10, v9, v21, s29
	v_dot2c_f32_f16_e32 v216, s4, v10
	v_and_b32_e32 v10, s32, v10
	v_dot2c_f32_f16_e32 v212, s4, v10
	v_perm_b32 v10, v9, v21, s30
	v_dot2c_f32_f16_e32 v217, s4, v10
	v_and_b32_e32 v10, s32, v10
	v_dot2c_f32_f16_e32 v213, s4, v10
	v_perm_b32 v10, v9, v21, s31
	v_perm_b32 v6, v9, v21, s33
	v_dot2c_f32_f16_e32 v214, s4, v10
	v_and_b32_e32 v10, s32, v10
	v_dot2c_f32_f16_e32 v215, s4, v6
	v_and_b32_e32 v6, s32, v6
	v_dot2c_f32_f16_e32 v218, s4, v11
	v_dot2c_f32_f16_e32 v210, s4, v10
	v_dot2c_f32_f16_e32 v211, s4, v6
	v_readlane_b32 s4, v254, 50
	buffer_load_dwordx4 v[18:21], v194, s[80:83], s76 offen
	buffer_load_dwordx4 v[6:9], v194, s[80:83], s77 offen
	v_perm_b32 v254, v4, v12, s29
	v_dot2c_f32_f16_e32 v224, s4, v254
	v_and_b32_e32 v254, s32, v254
	v_dot2c_f32_f16_e32 v220, s4, v254
	v_perm_b32 v254, v4, v12, s30
	v_dot2c_f32_f16_e32 v225, s4, v254
	v_and_b32_e32 v254, s32, v254
	v_dot2c_f32_f16_e32 v221, s4, v254
	v_perm_b32 v254, v4, v12, s31
	v_perm_b32 v3, v4, v12, s33
	v_dot2c_f32_f16_e32 v223, s4, v3
	v_and_b32_e32 v3, s32, v3
	v_dot2c_f32_f16_e32 v222, s4, v254
	v_and_b32_e32 v254, s32, v254
	v_dot2c_f32_f16_e32 v219, s4, v3
	v_perm_b32 v11, v5, v13, s29
	v_dot2c_f32_f16_e32 v216, s4, v11
	v_and_b32_e32 v11, s32, v11
	v_dot2c_f32_f16_e32 v212, s4, v11
	v_perm_b32 v11, v5, v13, s30
	v_dot2c_f32_f16_e32 v217, s4, v11
	v_and_b32_e32 v11, s32, v11
	v_dot2c_f32_f16_e32 v213, s4, v11
	v_perm_b32 v11, v5, v13, s31
	v_perm_b32 v3, v5, v13, s33
	v_dot2c_f32_f16_e32 v214, s4, v11
	v_and_b32_e32 v11, s32, v11
	v_dot2c_f32_f16_e32 v215, s4, v3
	v_and_b32_e32 v3, s32, v3
	v_dot2c_f32_f16_e32 v218, s4, v254
	v_dot2c_f32_f16_e32 v210, s4, v11
	v_dot2c_f32_f16_e32 v211, s4, v3
	buffer_load_dwordx4 v[10:13], v194, s[80:83], s78 offen
	buffer_load_dwordx4 v[2:5], v194, s[80:83], s79 offen
	v_add_f32_e32 v252, v68, v66
	s_add_i32 s21, s21, 32
	s_and_b64 vcc, exec, s[22:23]
	s_cbranch_vccnz .LBB0_1013
	s_waitcnt vmcnt(16)
	v_mov_b64_e32 v[158:159], v[112:113]
	v_mov_b64_e32 v[190:191], v[80:81]
	v_mov_b64_e32 v[186:187], v[76:77]
	v_mov_b64_e32 v[182:183], v[88:89]
	v_mov_b64_e32 v[178:179], v[84:85]
	v_mov_b64_e32 v[174:175], v[96:97]
	v_mov_b64_e32 v[170:171], v[92:93]
	v_mov_b64_e32 v[166:167], v[104:105]
	v_mov_b64_e32 v[162:163], v[100:101]
	v_mov_b64_e32 v[156:157], v[110:111]
	v_mov_b64_e32 v[154:155], v[108:109]
	v_mov_b64_e32 v[150:151], v[126:127]
	v_mov_b64_e32 v[146:147], v[122:123]
	v_mov_b64_e32 v[116:117], v[132:133]
	v_mov_b64_e32 v[112:113], v[128:129]
	v_mov_b64_e32 v[70:71], v[140:141]
	v_mov_b64_e32 v[66:67], v[136:137]
	v_mov_b64_e32 v[188:189], v[78:79]
	v_mov_b64_e32 v[184:185], v[74:75]
	v_mov_b64_e32 v[180:181], v[86:87]
	v_mov_b64_e32 v[176:177], v[82:83]
	v_mov_b64_e32 v[172:173], v[94:95]
	v_mov_b64_e32 v[168:169], v[90:91]
	v_mov_b64_e32 v[164:165], v[102:103]
	v_mov_b64_e32 v[160:161], v[98:99]
	v_mov_b64_e32 v[152:153], v[106:107]
	v_mov_b64_e32 v[148:149], v[124:125]
	v_mov_b64_e32 v[144:145], v[120:121]
	v_mov_b64_e32 v[118:119], v[134:135]
	v_mov_b64_e32 v[114:115], v[130:131]
	v_mov_b64_e32 v[72:73], v[142:143]
	v_mov_b64_e32 v[68:69], v[138:139]
	s_mov_b32 s25, s24
	s_branch .LBB0_1019

; #define LAS __attribute__((address_space(3)))
; #define EXP_XROW(tt) do { const char* g_ = (const char*)(xin + (size_t)(tt) * 1024) + lane * 16; LAS unsigned char* l_ = xslot + ((tt) & 1) * 2048; \
;         __builtin_amdgcn_global_load_lds((const unsigned*)g_, (LAS unsigned*)l_, 16, 0, 2); __builtin_amdgcn_global_load_lds((const unsigned*)(g_ + 1024), (LAS unsigned*)(l_ + 1024), 16, 0, 2); } while (0)
; __device__ __forceinline__ void expert_tokens(const unsigned char* __restrict__ UV, const float* __restrict__ US, const float* __restrict__ VS, ...
;     ...
;     for (int t = t0; t < t1; ++t) {
;         const bool has_next = t + 1 < t1; const int tn = has_next ? t + 1 : t;
;         const LAS float* pvt = pv; asm volatile("" : "+v"(pvt));
;         const unsigned nw0 = (unsigned)IDX[(size_t)tn * 128 + lane], nw1 = (unsigned)IDX[(size_t)tn * 128 + 64 + lane];
;         const int ni0 = (int)nw0 & rmask, ni1 = (int)nw1 & rmask;
;         const float ng0 = __uint_as_float(nw0 & 0xFFFF0000u), ng1 = __uint_as_float(nw1 & 0xFFFF0000u);
;         if (t == t0) asm volatile("s_waitcnt vmcnt(0)" ::: "memory"); else asm volatile("s_waitcnt vmcnt(32)" ::: "memory");
;         if (has_next) EXP_XROW(tn);
;         const LAS unsigned char* xrow = xslot + (t & 1) * 2048;
;         float nsu0 = 0.f, nsu1 = 0.f, nsv0 = 0.f, nsv1 = 0.f;
.LBB0_1024:
	s_waitcnt vmcnt(0)
	v_mul_f32_e32 v235, s16, v235
	v_mul_f32_e32 v236, s16, v236
	s_andn2_b64 vcc, exec, s[22:23]
	s_cbranch_vccz .LBB0_1017
	s_branch .LBB0_1018
